# in-proj epilogue: latent-norm weight loads waited once before any store; the 8 per-row-group vmcnt(0) store drains removed
# speedup vs baseline: 1.0139x; 1.0139x over previous
;     DEV void operator()(const pg8::Acc& acc, const pg8::Unit& u, int wr, int wc, int fr, int fq) const {
;         unsigned char* ws = p->ws; const int cb = u.pn * 256 + wc * 64;
;         f32x4 gq[2][2] = {};
;         if (cb >= 512 && cb < 1280) { const float* gain = (cb < 896 ? p->b_q_norm : p->b_k_norm) + layer * 64;
; #pragma unroll
;             for (int bj = 0; bj < 2; ++bj) { gq[bj][0] = *(const f32x4*)(gain + 32 * bj + 8 * fq); gq[bj][1] = *(const f32x4*)(gain + 32 * bj + 8 * fq + 4); } }
.LBB0_292:
	s_or_b32 s20, s8, s19
	s_waitcnt vmcnt(0)
	v_mov_b32_e32 v46, 0
	s_andn2_b64 vcc, exec, s[6:7]
	v_lshlrev_b32_e32 v149, 5, v148
	v_mov_b32_e32 v47, 0
	v_mov_b32_e32 v48, 0
	v_mov_b32_e32 v49, 0
	v_mov_b32_e32 v50, 0
	v_mov_b32_e32 v51, 0
	v_mov_b32_e32 v52, 0
	v_mov_b32_e32 v53, 0
	v_mov_b32_e32 v38, 0
	v_mov_b32_e32 v39, 0
	v_mov_b32_e32 v40, 0
	v_mov_b32_e32 v41, 0
	v_mov_b32_e32 v42, 0
	v_mov_b32_e32 v43, 0
	v_mov_b32_e32 v44, 0
	v_mov_b32_e32 v45, 0
	s_cbranch_vccnz .LBB0_294
	v_readlane_b32 s44, v254, 49
	s_cmpk_lt_i32 s20, 0x380
	v_readlane_b32 s46, v254, 51
	v_readlane_b32 s45, v254, 50
	v_readlane_b32 s47, v254, 52
	s_cselect_b32 s6, s44, s46
	s_cselect_b32 s7, s45, s47
	s_add_u32 s6, s6, s72
	s_addc_u32 s7, s7, s73
	global_load_dwordx4 v[46:49], v149, s[6:7]
	global_load_dwordx4 v[50:53], v149, s[6:7] offset:16
	global_load_dwordx4 v[38:41], v149, s[6:7] offset:128
	global_load_dwordx4 v[42:45], v149, s[6:7] offset:144
	s_waitcnt vmcnt(0)
	v_mov_b64_e32 v[146:147], v[178:179]

; DEV unsigned cvtpk(float lo, float hi) { f32x2 v = {lo, hi}; bf16v2 r = __builtin_convertvector(v, bf16v2); return __builtin_bit_cast(unsigned, r); }
; DEV float fast_rsq(float x) { return __builtin_amdgcn_rsqf(x); }
; DEV float lx16(float v) { return __builtin_bit_cast(float, __builtin_amdgcn_ds_swizzle(__builtin_bit_cast(int, v), 0x401F)); }
; DEV float half_sum(float v) { float a, b; swap32(v, a, b); return a + b; }
;     DEV void operator()(const pg8::Acc& acc, const pg8::Unit& u, int wr, int wc, int fr, int fq) const {
;     ...
;                 } else {
;                     float ss = 0.f;
; #pragma unroll
;                     for (int bj = 0; bj < 2; ++bj)
; #pragma unroll
;                         for (int e = 0; e < 8; ++e) ss += x[bj][e] * x[bj][e];
;                     ss += lx16(ss); ss = half_sum(ss);
;                     const float rinv = fast_rsq(ss * (1.0f / 64.0f) + EPS);
;                     const float sc = rinv * (sect == 0 ? 0.125f * LOG2E : 1.0f);
; #pragma unroll
;                     for (int bj = 0; bj < 2; ++bj) { const f32x4 g0 = gq[bj][0], g1 = gq[bj][1]; float y[8];
; #pragma unroll
;                         for (int e = 0; e < 4; ++e) { y[e] = x[bj][e] * sc * g0[e]; y[4 + e] = x[bj][4 + e] * sc * g1[e]; }
;                         const u32x4 w = {cvtpk(y[0], y[1]), cvtpk(y[2], y[3]), cvtpk(y[4], y[5]), cvtpk(y[6], y[7])};
;                         if (sect == 0) *(u32x4*)((bf16_t*)(ws + WS_QB) + (size_t)tok * 384 + hd * 64 + 32 * bj + 8 * fq) = w;
;                         else *(u32x4*)(ws + WS_KVB + ((size_t)((b * 6 + hd) * 260 + (kidx >> 6))) * 16384 + (4 * bj + fq) * 1024 + (kidx & 63) * 16) = w; }
.LBB0_299:
	s_andn2_b64 vcc, exec, s[20:21]
	s_cbranch_vccnz .LBB0_312
	s_mov_b32 s20, 0x8000
	v_and_b32_e32 v146, 0xcf, v176
	v_mov_b32_e32 v147, s75
	v_mov_b32_e32 v148, s88
	v_cmp_gt_i32_e32 vcc, s20, v176
	v_or_b32_e32 v146, 0x4000, v146
	s_mov_b64 s[20:21], -1
	v_cndmask_b32_e32 v177, v147, v148, vcc
	v_and_b32_e32 v147, 0x3fcf, v176
	v_cndmask_b32_e32 v167, v146, v147, vcc
	s_andn2_b64 vcc, exec, s[8:9]
	v_lshrrev_b32_e32 v182, 6, v167
	s_cbranch_vccnz .LBB0_310
	v_mul_f32_e32 v169, v143, v143
	v_fmac_f32_e32 v169, v142, v142
	v_fmac_f32_e32 v169, v144, v144
	v_fmac_f32_e32 v169, v145, v145
	v_fmac_f32_e32 v169, v138, v138
	v_fmac_f32_e32 v169, v139, v139
	v_fmac_f32_e32 v169, v140, v140
	v_fmac_f32_e32 v169, v141, v141
	v_fmac_f32_e32 v169, v134, v134
	v_fmac_f32_e32 v169, v135, v135
	v_fmac_f32_e32 v169, v136, v136
	v_fmac_f32_e32 v169, v137, v137
	v_pk_mul_f32 v[148:149], v[130:131], v[130:131]
	v_pk_mul_f32 v[146:147], v[132:133], v[132:133]
	v_add_f32_e32 v148, v148, v169
	v_add_f32_e32 v148, v149, v148
	v_add_f32_e32 v146, v146, v148
	v_add_f32_e32 v147, v147, v146
	ds_swizzle_b32 v148, v147 offset:swizzle(SWAP,16)
	v_mov_b32_e32 v146, s54
	s_and_b64 vcc, exec, s[6:7]
	s_waitcnt lgkmcnt(0)
	v_add_f32_e32 v147, v147, v148
	v_mov_b32_e32 v148, v147
	s_nop 1
	v_permlane32_swap_b32 v147, v148
	s_nop 1
	s_nop 0
	v_add_f32_e32 v147, v147, v148
	v_fmamk_f32 v147, v147, 0x3c800000, v0
	v_rsq_f32_e32 v148, v147
	v_mad_u64_u32 v[146:147], s[20:21], v177, 6, v[146:147]
	s_movk_i32 s20, 0x104
	s_nop 0
	v_mad_u64_u32 v[146:147], s[20:21], v146, s20, v[182:183]
	v_ashrrev_i32_e32 v147, 31, v146
	v_mul_f32_e32 v186, v191, v148
	v_lshlrev_b64 v[146:147], 14, v[146:147]
	v_lshlrev_b32_e32 v148, 4, v167
	v_lshl_add_u64 v[146:147], s[66:67], 0, v[146:147]
	v_and_b32_e32 v178, 0xf0, v148
	v_lshl_add_u64 v[184:185], v[146:147], 0, v[178:179]
	v_pk_mul_f32 v[146:147], v[142:143], v[186:187] op_sel_hi:[1,0]
	v_pk_mul_f32 v[148:149], v[138:139], v[186:187] op_sel_hi:[1,0]
	v_pk_mul_f32 v[188:189], v[144:145], v[186:187] op_sel_hi:[1,0]
	v_pk_mul_f32 v[194:195], v[140:141], v[186:187] op_sel_hi:[1,0]
	v_pk_mul_f32 v[146:147], v[46:47], v[146:147]
	v_pk_mul_f32 v[148:149], v[50:51], v[148:149]
	v_pk_mul_f32 v[188:189], v[48:49], v[188:189]
	v_pk_mul_f32 v[194:195], v[52:53], v[194:195]
	v_cvt_pk_bf16_f32 v146, v146, v147
	v_cvt_pk_bf16_f32 v147, v188, v189
	v_cvt_pk_bf16_f32 v148, v148, v149
	v_cvt_pk_bf16_f32 v149, v194, v195
	s_mov_b64 s[20:21], -1
	s_cbranch_vccz .LBB0_303
	v_mov_b32_e32 v169, v179
	v_lshl_add_u64 v[188:189], v[184:185], 0, v[168:169]
	global_store_dwordx4 v[188:189], v[146:149], off
	s_mov_b64 s[20:21], 0

; DEV unsigned cvtpk(float lo, float hi) { f32x2 v = {lo, hi}; bf16v2 r = __builtin_convertvector(v, bf16v2); return __builtin_bit_cast(unsigned, r); }
; DEV float fast_rsq(float x) { return __builtin_amdgcn_rsqf(x); }
; DEV float lx16(float v) { return __builtin_bit_cast(float, __builtin_amdgcn_ds_swizzle(__builtin_bit_cast(int, v), 0x401F)); }
; DEV float half_sum(float v) { float a, b; swap32(v, a, b); return a + b; }
;     DEV void operator()(const pg8::Acc& acc, const pg8::Unit& u, int wr, int wc, int fr, int fq) const {
;     ...
;                 } else {
;                     float ss = 0.f;
; #pragma unroll
;                     for (int bj = 0; bj < 2; ++bj)
; #pragma unroll
;                         for (int e = 0; e < 8; ++e) ss += x[bj][e] * x[bj][e];
;                     ss += lx16(ss); ss = half_sum(ss);
;                     const float rinv = fast_rsq(ss * (1.0f / 64.0f) + EPS);
;                     const float sc = rinv * (sect == 0 ? 0.125f * LOG2E : 1.0f);
; #pragma unroll
;                     for (int bj = 0; bj < 2; ++bj) { const f32x4 g0 = gq[bj][0], g1 = gq[bj][1]; float y[8];
; #pragma unroll
;                         for (int e = 0; e < 4; ++e) { y[e] = x[bj][e] * sc * g0[e]; y[4 + e] = x[bj][4 + e] * sc * g1[e]; }
;                         const u32x4 w = {cvtpk(y[0], y[1]), cvtpk(y[2], y[3]), cvtpk(y[4], y[5]), cvtpk(y[6], y[7])};
;                         if (sect == 0) *(u32x4*)((bf16_t*)(ws + WS_QB) + (size_t)tok * 384 + hd * 64 + 32 * bj + 8 * fq) = w;
;                         else *(u32x4*)(ws + WS_KVB + ((size_t)((b * 6 + hd) * 260 + (kidx >> 6))) * 16384 + (4 * bj + fq) * 1024 + (kidx & 63) * 16) = w; }
.LBB0_320:
	s_andn2_b64 vcc, exec, s[20:21]
	s_cbranch_vccnz .LBB0_333
	s_mov_b32 s20, 0x8000
	v_and_b32_e32 v130, 0xdf, v134
	v_mov_b32_e32 v131, s75
	v_mov_b32_e32 v132, s88
	v_cmp_gt_i32_e32 vcc, s20, v134
	v_or_b32_e32 v130, 0x4000, v130
	s_mov_b64 s[20:21], -1
	v_cndmask_b32_e32 v137, v131, v132, vcc
	v_and_b32_e32 v131, 0x3fdf, v134
	v_cndmask_b32_e32 v135, v130, v131, vcc
	s_andn2_b64 vcc, exec, s[8:9]
	v_lshrrev_b32_e32 v136, 6, v135
	s_cbranch_vccnz .LBB0_331
	v_mul_f32_e32 v138, v127, v127
	v_fmac_f32_e32 v138, v126, v126
	v_fmac_f32_e32 v138, v128, v128
	v_fmac_f32_e32 v138, v129, v129
	v_fmac_f32_e32 v138, v122, v122
	v_fmac_f32_e32 v138, v123, v123
	v_fmac_f32_e32 v138, v124, v124
	v_fmac_f32_e32 v138, v125, v125
	v_fmac_f32_e32 v138, v118, v118
	v_fmac_f32_e32 v138, v119, v119
	v_fmac_f32_e32 v138, v120, v120
	v_fmac_f32_e32 v138, v121, v121
	v_pk_mul_f32 v[132:133], v[114:115], v[114:115]
	v_pk_mul_f32 v[130:131], v[116:117], v[116:117]
	v_add_f32_e32 v132, v132, v138
	v_add_f32_e32 v132, v133, v132
	v_add_f32_e32 v130, v130, v132
	v_add_f32_e32 v131, v131, v130
	ds_swizzle_b32 v132, v131 offset:swizzle(SWAP,16)
	v_mov_b32_e32 v130, s54
	s_andn2_b64 vcc, exec, s[6:7]
	s_waitcnt lgkmcnt(0)
	v_add_f32_e32 v131, v131, v132
	v_mov_b32_e32 v132, v131
	s_nop 1
	v_permlane32_swap_b32 v131, v132
	s_nop 1
	s_nop 0
	v_add_f32_e32 v131, v131, v132
	v_fmamk_f32 v131, v131, 0x3c800000, v0
	v_rsq_f32_e32 v132, v131
	v_mad_u64_u32 v[130:131], s[20:21], v137, 6, v[130:131]
	s_movk_i32 s20, 0x104
	s_nop 0
	v_mad_u64_u32 v[130:131], s[20:21], v130, s20, v[136:137]
	v_ashrrev_i32_e32 v131, 31, v130
	v_mul_f32_e32 v140, v191, v132
	v_lshlrev_b64 v[130:131], 14, v[130:131]
	v_lshlrev_b32_e32 v132, 4, v135
	v_lshl_add_u64 v[130:131], s[66:67], 0, v[130:131]
	v_and_b32_e32 v178, 0x1f0, v132
	v_lshl_add_u64 v[138:139], v[130:131], 0, v[178:179]
	v_pk_mul_f32 v[130:131], v[126:127], v[140:141] op_sel_hi:[1,0]
	v_pk_mul_f32 v[132:133], v[122:123], v[140:141] op_sel_hi:[1,0]
	v_pk_mul_f32 v[142:143], v[128:129], v[140:141] op_sel_hi:[1,0]
	v_pk_mul_f32 v[144:145], v[124:125], v[140:141] op_sel_hi:[1,0]
	v_pk_mul_f32 v[130:131], v[46:47], v[130:131]
	v_pk_mul_f32 v[132:133], v[50:51], v[132:133]
	v_pk_mul_f32 v[142:143], v[48:49], v[142:143]
	v_pk_mul_f32 v[144:145], v[52:53], v[144:145]
	v_cndmask_b32_e64 v141, 0, 1, s[6:7]
	v_cvt_pk_bf16_f32 v130, v130, v131
	v_cvt_pk_bf16_f32 v131, v142, v143
	v_cvt_pk_bf16_f32 v132, v132, v133
	v_cvt_pk_bf16_f32 v133, v144, v145
	v_cmp_ne_u32_e64 s[48:49], 1, v141
	s_mov_b64 s[20:21], -1
	s_cbranch_vccnz .LBB0_324
	v_mov_b32_e32 v169, v179
	v_lshl_add_u64 v[142:143], v[138:139], 0, v[168:169]
	s_mov_b64 s[20:21], 0
	global_store_dwordx4 v[142:143], v[130:133], off

; DEV unsigned cvtpk(float lo, float hi) { f32x2 v = {lo, hi}; bf16v2 r = __builtin_convertvector(v, bf16v2); return __builtin_bit_cast(unsigned, r); }
; DEV float fast_rsq(float x) { return __builtin_amdgcn_rsqf(x); }
; DEV float lx16(float v) { return __builtin_bit_cast(float, __builtin_amdgcn_ds_swizzle(__builtin_bit_cast(int, v), 0x401F)); }
; DEV float half_sum(float v) { float a, b; swap32(v, a, b); return a + b; }
;     DEV void operator()(const pg8::Acc& acc, const pg8::Unit& u, int wr, int wc, int fr, int fq) const {
;     ...
;                 } else {
;                     float ss = 0.f;
; #pragma unroll
;                     for (int bj = 0; bj < 2; ++bj)
; #pragma unroll
;                         for (int e = 0; e < 8; ++e) ss += x[bj][e] * x[bj][e];
;                     ss += lx16(ss); ss = half_sum(ss);
;                     const float rinv = fast_rsq(ss * (1.0f / 64.0f) + EPS);
;                     const float sc = rinv * (sect == 0 ? 0.125f * LOG2E : 1.0f);
; #pragma unroll
;                     for (int bj = 0; bj < 2; ++bj) { const f32x4 g0 = gq[bj][0], g1 = gq[bj][1]; float y[8];
; #pragma unroll
;                         for (int e = 0; e < 4; ++e) { y[e] = x[bj][e] * sc * g0[e]; y[4 + e] = x[bj][4 + e] * sc * g1[e]; }
;                         const u32x4 w = {cvtpk(y[0], y[1]), cvtpk(y[2], y[3]), cvtpk(y[4], y[5]), cvtpk(y[6], y[7])};
;                         if (sect == 0) *(u32x4*)((bf16_t*)(ws + WS_QB) + (size_t)tok * 384 + hd * 64 + 32 * bj + 8 * fq) = w;
;                         else *(u32x4*)(ws + WS_KVB + ((size_t)((b * 6 + hd) * 260 + (kidx >> 6))) * 16384 + (4 * bj + fq) * 1024 + (kidx & 63) * 16) = w; }
.LBB0_339:
	s_andn2_b64 vcc, exec, s[20:21]
	s_cbranch_vccnz .LBB0_352
	s_mov_b32 s20, 0x8000
	v_and_b32_e32 v114, 0xef, v118
	v_mov_b32_e32 v115, s75
	v_mov_b32_e32 v116, s88
	v_cmp_gt_i32_e32 vcc, s20, v118
	v_or_b32_e32 v114, 0x4000, v114
	s_mov_b64 s[20:21], -1
	v_cndmask_b32_e32 v121, v115, v116, vcc
	v_and_b32_e32 v115, 0x3fef, v118
	v_cndmask_b32_e32 v119, v114, v115, vcc
	s_andn2_b64 vcc, exec, s[8:9]
	v_lshrrev_b32_e32 v120, 6, v119
	s_cbranch_vccnz .LBB0_350
	v_mul_f32_e32 v122, v111, v111
	v_fmac_f32_e32 v122, v110, v110
	v_fmac_f32_e32 v122, v112, v112
	v_fmac_f32_e32 v122, v113, v113
	v_fmac_f32_e32 v122, v106, v106
	v_fmac_f32_e32 v122, v107, v107
	v_fmac_f32_e32 v122, v108, v108
	v_fmac_f32_e32 v122, v109, v109
	v_fmac_f32_e32 v122, v102, v102
	v_fmac_f32_e32 v122, v103, v103
	v_fmac_f32_e32 v122, v104, v104
	v_fmac_f32_e32 v122, v105, v105
	v_pk_mul_f32 v[116:117], v[98:99], v[98:99]
	v_pk_mul_f32 v[114:115], v[100:101], v[100:101]
	v_add_f32_e32 v116, v116, v122
	v_add_f32_e32 v116, v117, v116
	v_add_f32_e32 v114, v114, v116
	v_add_f32_e32 v115, v115, v114
	ds_swizzle_b32 v116, v115 offset:swizzle(SWAP,16)
	v_mov_b32_e32 v114, s54
	s_andn2_b64 vcc, exec, s[6:7]
	s_waitcnt lgkmcnt(0)
	v_add_f32_e32 v115, v115, v116
	v_mov_b32_e32 v116, v115
	s_nop 1
	v_permlane32_swap_b32 v115, v116
	s_nop 1
	s_nop 0
	v_add_f32_e32 v115, v115, v116
	v_fmamk_f32 v115, v115, 0x3c800000, v0
	v_rsq_f32_e32 v116, v115
	v_mad_u64_u32 v[114:115], s[20:21], v121, 6, v[114:115]
	s_movk_i32 s20, 0x104
	s_nop 0
	v_mad_u64_u32 v[114:115], s[20:21], v114, s20, v[120:121]
	v_ashrrev_i32_e32 v115, 31, v114
	v_mul_f32_e32 v124, v191, v116
	v_lshlrev_b64 v[114:115], 14, v[114:115]
	v_lshlrev_b32_e32 v116, 4, v119
	v_lshl_add_u64 v[114:115], s[66:67], 0, v[114:115]
	v_and_b32_e32 v178, 0x2f0, v116
	v_lshl_add_u64 v[122:123], v[114:115], 0, v[178:179]
	v_pk_mul_f32 v[114:115], v[110:111], v[124:125] op_sel_hi:[1,0]
	v_pk_mul_f32 v[116:117], v[106:107], v[124:125] op_sel_hi:[1,0]
	v_pk_mul_f32 v[126:127], v[112:113], v[124:125] op_sel_hi:[1,0]
	v_pk_mul_f32 v[128:129], v[108:109], v[124:125] op_sel_hi:[1,0]
	v_pk_mul_f32 v[114:115], v[46:47], v[114:115]
	v_pk_mul_f32 v[116:117], v[50:51], v[116:117]
	v_pk_mul_f32 v[126:127], v[48:49], v[126:127]
	v_pk_mul_f32 v[128:129], v[52:53], v[128:129]
	v_cndmask_b32_e64 v125, 0, 1, s[6:7]
	v_cvt_pk_bf16_f32 v114, v114, v115
	v_cvt_pk_bf16_f32 v115, v126, v127
	v_cvt_pk_bf16_f32 v116, v116, v117
	v_cvt_pk_bf16_f32 v117, v128, v129
	v_cmp_ne_u32_e64 s[48:49], 1, v125
	s_mov_b64 s[20:21], -1
	s_cbranch_vccnz .LBB0_343
	v_mov_b32_e32 v169, v179
	v_lshl_add_u64 v[126:127], v[122:123], 0, v[168:169]
	s_mov_b64 s[20:21], 0
	global_store_dwordx4 v[126:127], v[114:117], off

; DEV unsigned cvtpk(float lo, float hi) { f32x2 v = {lo, hi}; bf16v2 r = __builtin_convertvector(v, bf16v2); return __builtin_bit_cast(unsigned, r); }
; DEV float fast_rsq(float x) { return __builtin_amdgcn_rsqf(x); }
; DEV float lx16(float v) { return __builtin_bit_cast(float, __builtin_amdgcn_ds_swizzle(__builtin_bit_cast(int, v), 0x401F)); }
; DEV float half_sum(float v) { float a, b; swap32(v, a, b); return a + b; }
;     DEV void operator()(const pg8::Acc& acc, const pg8::Unit& u, int wr, int wc, int fr, int fq) const {
;     ...
;                 } else {
;                     float ss = 0.f;
; #pragma unroll
;                     for (int bj = 0; bj < 2; ++bj)
; #pragma unroll
;                         for (int e = 0; e < 8; ++e) ss += x[bj][e] * x[bj][e];
;                     ss += lx16(ss); ss = half_sum(ss);
;                     const float rinv = fast_rsq(ss * (1.0f / 64.0f) + EPS);
;                     const float sc = rinv * (sect == 0 ? 0.125f * LOG2E : 1.0f);
; #pragma unroll
;                     for (int bj = 0; bj < 2; ++bj) { const f32x4 g0 = gq[bj][0], g1 = gq[bj][1]; float y[8];
; #pragma unroll
;                         for (int e = 0; e < 4; ++e) { y[e] = x[bj][e] * sc * g0[e]; y[4 + e] = x[bj][4 + e] * sc * g1[e]; }
;                         const u32x4 w = {cvtpk(y[0], y[1]), cvtpk(y[2], y[3]), cvtpk(y[4], y[5]), cvtpk(y[6], y[7])};
;                         if (sect == 0) *(u32x4*)((bf16_t*)(ws + WS_QB) + (size_t)tok * 384 + hd * 64 + 32 * bj + 8 * fq) = w;
;                         else *(u32x4*)(ws + WS_KVB + ((size_t)((b * 6 + hd) * 260 + (kidx >> 6))) * 16384 + (4 * bj + fq) * 1024 + (kidx & 63) * 16) = w; }
.LBB0_358:
	s_andn2_b64 vcc, exec, s[20:21]
	s_cbranch_vccnz .LBB0_371
	s_mov_b32 s20, 0x8000
	v_mov_b32_e32 v98, s75
	v_mov_b32_e32 v99, s88
	v_cmp_gt_i32_e32 vcc, s20, v102
	s_movk_i32 s20, 0x4000
	s_nop 0
	v_cndmask_b32_e32 v105, v98, v99, vcc
	v_and_b32_e32 v98, 0x3fff, v102
	v_or_b32_sdwa v99, v102, s20 dst_sel:DWORD dst_unused:UNUSED_PAD src0_sel:BYTE_0 src1_sel:DWORD
	v_cndmask_b32_e32 v103, v99, v98, vcc
	s_mov_b64 s[20:21], -1
	s_andn2_b64 vcc, exec, s[8:9]
	v_lshrrev_b32_e32 v104, 6, v103
	s_cbranch_vccnz .LBB0_369
	v_mul_f32_e32 v106, v95, v95
	v_fmac_f32_e32 v106, v94, v94
	v_fmac_f32_e32 v106, v96, v96
	v_fmac_f32_e32 v106, v97, v97
	v_fmac_f32_e32 v106, v90, v90
	v_fmac_f32_e32 v106, v91, v91
	v_fmac_f32_e32 v106, v92, v92
	v_fmac_f32_e32 v106, v93, v93
	v_fmac_f32_e32 v106, v86, v86
	v_fmac_f32_e32 v106, v87, v87
	v_fmac_f32_e32 v106, v88, v88
	v_fmac_f32_e32 v106, v89, v89
	v_pk_mul_f32 v[100:101], v[82:83], v[82:83]
	v_pk_mul_f32 v[98:99], v[84:85], v[84:85]
	v_add_f32_e32 v100, v100, v106
	v_add_f32_e32 v100, v101, v100
	v_add_f32_e32 v98, v98, v100
	v_add_f32_e32 v99, v99, v98
	ds_swizzle_b32 v100, v99 offset:swizzle(SWAP,16)
	v_mov_b32_e32 v98, s54
	s_andn2_b64 vcc, exec, s[6:7]
	s_waitcnt lgkmcnt(0)
	v_add_f32_e32 v99, v99, v100
	v_mov_b32_e32 v100, v99
	s_nop 1
	v_permlane32_swap_b32 v99, v100
	s_nop 1
	s_nop 0
	v_add_f32_e32 v99, v99, v100
	v_fmamk_f32 v99, v99, 0x3c800000, v0
	v_rsq_f32_e32 v100, v99
	v_mad_u64_u32 v[98:99], s[20:21], v105, 6, v[98:99]
	s_movk_i32 s20, 0x104
	s_nop 0
	v_mad_u64_u32 v[98:99], s[20:21], v98, s20, v[104:105]
	v_ashrrev_i32_e32 v99, 31, v98
	v_mul_f32_e32 v108, v191, v100
	v_lshlrev_b64 v[98:99], 14, v[98:99]
	v_lshlrev_b32_e32 v100, 4, v103
	v_lshl_add_u64 v[98:99], s[66:67], 0, v[98:99]
	v_and_b32_e32 v178, 0x3f0, v100
	v_lshl_add_u64 v[106:107], v[98:99], 0, v[178:179]
	v_pk_mul_f32 v[98:99], v[94:95], v[108:109] op_sel_hi:[1,0]
	v_pk_mul_f32 v[100:101], v[90:91], v[108:109] op_sel_hi:[1,0]
	v_pk_mul_f32 v[110:111], v[96:97], v[108:109] op_sel_hi:[1,0]
	v_pk_mul_f32 v[112:113], v[92:93], v[108:109] op_sel_hi:[1,0]
	v_pk_mul_f32 v[98:99], v[46:47], v[98:99]
	v_pk_mul_f32 v[100:101], v[50:51], v[100:101]
	v_pk_mul_f32 v[110:111], v[48:49], v[110:111]
	v_pk_mul_f32 v[112:113], v[52:53], v[112:113]
	v_cndmask_b32_e64 v109, 0, 1, s[6:7]
	v_cvt_pk_bf16_f32 v98, v98, v99
	v_cvt_pk_bf16_f32 v99, v110, v111
	v_cvt_pk_bf16_f32 v100, v100, v101
	v_cvt_pk_bf16_f32 v101, v112, v113
	v_cmp_ne_u32_e64 s[48:49], 1, v109
	s_mov_b64 s[20:21], -1
	s_cbranch_vccnz .LBB0_362
	v_mov_b32_e32 v169, v179
	v_lshl_add_u64 v[110:111], v[106:107], 0, v[168:169]
	s_mov_b64 s[20:21], 0
	global_store_dwordx4 v[110:111], v[98:101], off

; DEV unsigned cvtpk(float lo, float hi) { f32x2 v = {lo, hi}; bf16v2 r = __builtin_convertvector(v, bf16v2); return __builtin_bit_cast(unsigned, r); }
; DEV float fast_rsq(float x) { return __builtin_amdgcn_rsqf(x); }
; DEV float lx16(float v) { return __builtin_bit_cast(float, __builtin_amdgcn_ds_swizzle(__builtin_bit_cast(int, v), 0x401F)); }
; DEV float half_sum(float v) { float a, b; swap32(v, a, b); return a + b; }
;     DEV void operator()(const pg8::Acc& acc, const pg8::Unit& u, int wr, int wc, int fr, int fq) const {
;     ...
;                 } else {
;                     float ss = 0.f;
; #pragma unroll
;                     for (int bj = 0; bj < 2; ++bj)
; #pragma unroll
;                         for (int e = 0; e < 8; ++e) ss += x[bj][e] * x[bj][e];
;                     ss += lx16(ss); ss = half_sum(ss);
;                     const float rinv = fast_rsq(ss * (1.0f / 64.0f) + EPS);
;                     const float sc = rinv * (sect == 0 ? 0.125f * LOG2E : 1.0f);
; #pragma unroll
;                     for (int bj = 0; bj < 2; ++bj) { const f32x4 g0 = gq[bj][0], g1 = gq[bj][1]; float y[8];
; #pragma unroll
;                         for (int e = 0; e < 4; ++e) { y[e] = x[bj][e] * sc * g0[e]; y[4 + e] = x[bj][4 + e] * sc * g1[e]; }
;                         const u32x4 w = {cvtpk(y[0], y[1]), cvtpk(y[2], y[3]), cvtpk(y[4], y[5]), cvtpk(y[6], y[7])};
;                         if (sect == 0) *(u32x4*)((bf16_t*)(ws + WS_QB) + (size_t)tok * 384 + hd * 64 + 32 * bj + 8 * fq) = w;
;                         else *(u32x4*)(ws + WS_KVB + ((size_t)((b * 6 + hd) * 260 + (kidx >> 6))) * 16384 + (4 * bj + fq) * 1024 + (kidx & 63) * 16) = w; }
.LBB0_383:
	s_andn2_b64 vcc, exec, s[20:21]
	s_cbranch_vccnz .LBB0_396
	s_mov_b32 s20, 0x8000
	v_and_b32_e32 v82, 0xcf, v86
	v_mov_b32_e32 v83, s55
	v_mov_b32_e32 v84, s58
	v_cmp_gt_i32_e32 vcc, s20, v86
	v_or_b32_e32 v82, 0x4000, v82
	s_mov_b64 s[20:21], -1
	v_cndmask_b32_e32 v89, v83, v84, vcc
	v_and_b32_e32 v83, 0x3fcf, v86
	v_cndmask_b32_e32 v87, v82, v83, vcc
	s_andn2_b64 vcc, exec, s[8:9]
	v_lshrrev_b32_e32 v88, 6, v87
	s_cbranch_vccnz .LBB0_394
	v_mul_f32_e32 v90, v79, v79
	v_fmac_f32_e32 v90, v78, v78
	v_fmac_f32_e32 v90, v80, v80
	v_fmac_f32_e32 v90, v81, v81
	v_fmac_f32_e32 v90, v74, v74
	v_fmac_f32_e32 v90, v75, v75
	v_fmac_f32_e32 v90, v76, v76
	v_fmac_f32_e32 v90, v77, v77
	v_fmac_f32_e32 v90, v70, v70
	v_fmac_f32_e32 v90, v71, v71
	v_fmac_f32_e32 v90, v72, v72
	v_fmac_f32_e32 v90, v73, v73
	v_pk_mul_f32 v[84:85], v[66:67], v[66:67]
	v_pk_mul_f32 v[82:83], v[68:69], v[68:69]
	v_add_f32_e32 v84, v84, v90
	v_add_f32_e32 v84, v85, v84
	v_add_f32_e32 v82, v82, v84
	v_add_f32_e32 v83, v83, v82
	ds_swizzle_b32 v84, v83 offset:swizzle(SWAP,16)
	v_mov_b32_e32 v82, s54
	s_andn2_b64 vcc, exec, s[6:7]
	s_waitcnt lgkmcnt(0)
	v_add_f32_e32 v83, v83, v84
	v_mov_b32_e32 v84, v83
	s_nop 1
	v_permlane32_swap_b32 v83, v84
	s_nop 1
	s_nop 0
	v_add_f32_e32 v83, v83, v84
	v_fmamk_f32 v83, v83, 0x3c800000, v0
	v_rsq_f32_e32 v84, v83
	v_mad_u64_u32 v[82:83], s[20:21], v89, 6, v[82:83]
	s_movk_i32 s20, 0x104
	s_nop 0
	v_mad_u64_u32 v[82:83], s[20:21], v82, s20, v[88:89]
	v_ashrrev_i32_e32 v83, 31, v82
	v_mul_f32_e32 v92, v191, v84
	v_lshlrev_b64 v[82:83], 14, v[82:83]
	v_lshlrev_b32_e32 v84, 4, v87
	v_lshl_add_u64 v[82:83], s[66:67], 0, v[82:83]
	v_and_b32_e32 v178, 0xf0, v84
	v_lshl_add_u64 v[90:91], v[82:83], 0, v[178:179]
	v_pk_mul_f32 v[82:83], v[78:79], v[92:93] op_sel_hi:[1,0]
	v_pk_mul_f32 v[84:85], v[74:75], v[92:93] op_sel_hi:[1,0]
	v_pk_mul_f32 v[94:95], v[80:81], v[92:93] op_sel_hi:[1,0]
	v_pk_mul_f32 v[96:97], v[76:77], v[92:93] op_sel_hi:[1,0]
	v_pk_mul_f32 v[82:83], v[46:47], v[82:83]
	v_pk_mul_f32 v[84:85], v[50:51], v[84:85]
	v_pk_mul_f32 v[94:95], v[48:49], v[94:95]
	v_pk_mul_f32 v[96:97], v[52:53], v[96:97]
	v_cndmask_b32_e64 v93, 0, 1, s[6:7]
	v_cvt_pk_bf16_f32 v82, v82, v83
	v_cvt_pk_bf16_f32 v83, v94, v95
	v_cvt_pk_bf16_f32 v84, v84, v85
	v_cvt_pk_bf16_f32 v85, v96, v97
	v_cmp_ne_u32_e64 s[48:49], 1, v93
	s_mov_b64 s[20:21], -1
	s_cbranch_vccnz .LBB0_387
	v_mov_b32_e32 v169, v179
	v_lshl_add_u64 v[94:95], v[90:91], 0, v[168:169]
	s_mov_b64 s[20:21], 0
	global_store_dwordx4 v[94:95], v[82:85], off

; DEV unsigned cvtpk(float lo, float hi) { f32x2 v = {lo, hi}; bf16v2 r = __builtin_convertvector(v, bf16v2); return __builtin_bit_cast(unsigned, r); }
; DEV float fast_rsq(float x) { return __builtin_amdgcn_rsqf(x); }
; DEV float lx16(float v) { return __builtin_bit_cast(float, __builtin_amdgcn_ds_swizzle(__builtin_bit_cast(int, v), 0x401F)); }
; DEV float half_sum(float v) { float a, b; swap32(v, a, b); return a + b; }
;     DEV void operator()(const pg8::Acc& acc, const pg8::Unit& u, int wr, int wc, int fr, int fq) const {
;     ...
;                 } else {
;                     float ss = 0.f;
; #pragma unroll
;                     for (int bj = 0; bj < 2; ++bj)
; #pragma unroll
;                         for (int e = 0; e < 8; ++e) ss += x[bj][e] * x[bj][e];
;                     ss += lx16(ss); ss = half_sum(ss);
;                     const float rinv = fast_rsq(ss * (1.0f / 64.0f) + EPS);
;                     const float sc = rinv * (sect == 0 ? 0.125f * LOG2E : 1.0f);
; #pragma unroll
;                     for (int bj = 0; bj < 2; ++bj) { const f32x4 g0 = gq[bj][0], g1 = gq[bj][1]; float y[8];
; #pragma unroll
;                         for (int e = 0; e < 4; ++e) { y[e] = x[bj][e] * sc * g0[e]; y[4 + e] = x[bj][4 + e] * sc * g1[e]; }
;                         const u32x4 w = {cvtpk(y[0], y[1]), cvtpk(y[2], y[3]), cvtpk(y[4], y[5]), cvtpk(y[6], y[7])};
;                         if (sect == 0) *(u32x4*)((bf16_t*)(ws + WS_QB) + (size_t)tok * 384 + hd * 64 + 32 * bj + 8 * fq) = w;
;                         else *(u32x4*)(ws + WS_KVB + ((size_t)((b * 6 + hd) * 260 + (kidx >> 6))) * 16384 + (4 * bj + fq) * 1024 + (kidx & 63) * 16) = w; }
.LBB0_402:
	s_andn2_b64 vcc, exec, s[20:21]
	s_cbranch_vccnz .LBB0_415
	s_mov_b32 s20, 0x8000
	v_and_b32_e32 v66, 0xdf, v70
	v_mov_b32_e32 v67, s55
	v_mov_b32_e32 v68, s58
	v_cmp_gt_i32_e32 vcc, s20, v70
	v_or_b32_e32 v66, 0x4000, v66
	s_mov_b64 s[20:21], -1
	v_cndmask_b32_e32 v73, v67, v68, vcc
	v_and_b32_e32 v67, 0x3fdf, v70
	v_cndmask_b32_e32 v71, v66, v67, vcc
	s_andn2_b64 vcc, exec, s[8:9]
	v_lshrrev_b32_e32 v72, 6, v71
	s_cbranch_vccnz .LBB0_413
	v_mul_f32_e32 v74, v63, v63
	v_fmac_f32_e32 v74, v62, v62
	v_fmac_f32_e32 v74, v64, v64
	v_fmac_f32_e32 v74, v65, v65
	v_fmac_f32_e32 v74, v58, v58
	v_fmac_f32_e32 v74, v59, v59
	v_fmac_f32_e32 v74, v60, v60
	v_fmac_f32_e32 v74, v61, v61
	v_fmac_f32_e32 v74, v54, v54
	v_fmac_f32_e32 v74, v55, v55
	v_fmac_f32_e32 v74, v56, v56
	v_fmac_f32_e32 v74, v57, v57
	v_pk_mul_f32 v[68:69], v[34:35], v[34:35]
	v_pk_mul_f32 v[66:67], v[36:37], v[36:37]
	v_add_f32_e32 v68, v68, v74
	v_add_f32_e32 v68, v69, v68
	v_add_f32_e32 v66, v66, v68
	v_add_f32_e32 v67, v67, v66
	ds_swizzle_b32 v68, v67 offset:swizzle(SWAP,16)
	v_mov_b32_e32 v66, s54
	s_andn2_b64 vcc, exec, s[6:7]
	s_waitcnt lgkmcnt(0)
	v_add_f32_e32 v67, v67, v68
	v_mov_b32_e32 v68, v67
	s_nop 1
	v_permlane32_swap_b32 v67, v68
	s_nop 1
	s_nop 0
	v_add_f32_e32 v67, v67, v68
	v_fmamk_f32 v67, v67, 0x3c800000, v0
	v_rsq_f32_e32 v68, v67
	v_mad_u64_u32 v[66:67], s[20:21], v73, 6, v[66:67]
	s_movk_i32 s20, 0x104
	s_nop 0
	v_mad_u64_u32 v[66:67], s[20:21], v66, s20, v[72:73]
	v_ashrrev_i32_e32 v67, 31, v66
	v_mul_f32_e32 v76, v191, v68
	v_lshlrev_b64 v[66:67], 14, v[66:67]
	v_lshlrev_b32_e32 v68, 4, v71
	v_lshl_add_u64 v[66:67], s[66:67], 0, v[66:67]
	v_and_b32_e32 v178, 0x1f0, v68
	v_lshl_add_u64 v[74:75], v[66:67], 0, v[178:179]
	v_pk_mul_f32 v[66:67], v[62:63], v[76:77] op_sel_hi:[1,0]
	v_pk_mul_f32 v[68:69], v[58:59], v[76:77] op_sel_hi:[1,0]
	v_pk_mul_f32 v[78:79], v[64:65], v[76:77] op_sel_hi:[1,0]
	v_pk_mul_f32 v[80:81], v[60:61], v[76:77] op_sel_hi:[1,0]
	v_pk_mul_f32 v[66:67], v[46:47], v[66:67]
	v_pk_mul_f32 v[68:69], v[50:51], v[68:69]
	v_pk_mul_f32 v[78:79], v[48:49], v[78:79]
	v_pk_mul_f32 v[80:81], v[52:53], v[80:81]
	v_cndmask_b32_e64 v77, 0, 1, s[6:7]
	v_cvt_pk_bf16_f32 v66, v66, v67
	v_cvt_pk_bf16_f32 v67, v78, v79
	v_cvt_pk_bf16_f32 v68, v68, v69
	v_cvt_pk_bf16_f32 v69, v80, v81
	v_cmp_ne_u32_e64 s[48:49], 1, v77
	s_mov_b64 s[20:21], -1
	s_cbranch_vccnz .LBB0_406
	v_mov_b32_e32 v169, v179
	v_lshl_add_u64 v[78:79], v[74:75], 0, v[168:169]
	s_mov_b64 s[20:21], 0
	global_store_dwordx4 v[78:79], v[66:69], off

; DEV unsigned cvtpk(float lo, float hi) { f32x2 v = {lo, hi}; bf16v2 r = __builtin_convertvector(v, bf16v2); return __builtin_bit_cast(unsigned, r); }
; DEV float fast_rsq(float x) { return __builtin_amdgcn_rsqf(x); }
; DEV float lx16(float v) { return __builtin_bit_cast(float, __builtin_amdgcn_ds_swizzle(__builtin_bit_cast(int, v), 0x401F)); }
; DEV float half_sum(float v) { float a, b; swap32(v, a, b); return a + b; }
;     DEV void operator()(const pg8::Acc& acc, const pg8::Unit& u, int wr, int wc, int fr, int fq) const {
;     ...
;                 } else {
;                     float ss = 0.f;
; #pragma unroll
;                     for (int bj = 0; bj < 2; ++bj)
; #pragma unroll
;                         for (int e = 0; e < 8; ++e) ss += x[bj][e] * x[bj][e];
;                     ss += lx16(ss); ss = half_sum(ss);
;                     const float rinv = fast_rsq(ss * (1.0f / 64.0f) + EPS);
;                     const float sc = rinv * (sect == 0 ? 0.125f * LOG2E : 1.0f);
; #pragma unroll
;                     for (int bj = 0; bj < 2; ++bj) { const f32x4 g0 = gq[bj][0], g1 = gq[bj][1]; float y[8];
; #pragma unroll
;                         for (int e = 0; e < 4; ++e) { y[e] = x[bj][e] * sc * g0[e]; y[4 + e] = x[bj][4 + e] * sc * g1[e]; }
;                         const u32x4 w = {cvtpk(y[0], y[1]), cvtpk(y[2], y[3]), cvtpk(y[4], y[5]), cvtpk(y[6], y[7])};
;                         if (sect == 0) *(u32x4*)((bf16_t*)(ws + WS_QB) + (size_t)tok * 384 + hd * 64 + 32 * bj + 8 * fq) = w;
;                         else *(u32x4*)(ws + WS_KVB + ((size_t)((b * 6 + hd) * 260 + (kidx >> 6))) * 16384 + (4 * bj + fq) * 1024 + (kidx & 63) * 16) = w; }
.LBB0_421:
	s_andn2_b64 vcc, exec, s[20:21]
	s_cbranch_vccnz .LBB0_434
	s_mov_b32 s20, 0x8000
	v_and_b32_e32 v34, 0xef, v54
	v_mov_b32_e32 v35, s55
	v_mov_b32_e32 v36, s58
	v_cmp_gt_i32_e32 vcc, s20, v54
	v_or_b32_e32 v34, 0x4000, v34
	s_mov_b64 s[20:21], -1
	v_cndmask_b32_e32 v57, v35, v36, vcc
	v_and_b32_e32 v35, 0x3fef, v54
	v_cndmask_b32_e32 v55, v34, v35, vcc
	s_andn2_b64 vcc, exec, s[8:9]
	v_lshrrev_b32_e32 v56, 6, v55
	s_cbranch_vccnz .LBB0_432
	v_mul_f32_e32 v58, v31, v31
	v_fmac_f32_e32 v58, v30, v30
	v_fmac_f32_e32 v58, v32, v32
	v_fmac_f32_e32 v58, v33, v33
	v_fmac_f32_e32 v58, v26, v26
	v_fmac_f32_e32 v58, v27, v27
	v_fmac_f32_e32 v58, v28, v28
	v_fmac_f32_e32 v58, v29, v29
	v_fmac_f32_e32 v58, v22, v22
	v_fmac_f32_e32 v58, v23, v23
	v_fmac_f32_e32 v58, v24, v24
	v_fmac_f32_e32 v58, v25, v25
	v_pk_mul_f32 v[36:37], v[18:19], v[18:19]
	v_pk_mul_f32 v[34:35], v[20:21], v[20:21]
	v_add_f32_e32 v36, v36, v58
	v_add_f32_e32 v36, v37, v36
	v_add_f32_e32 v34, v34, v36
	v_add_f32_e32 v35, v35, v34
	ds_swizzle_b32 v36, v35 offset:swizzle(SWAP,16)
	v_mov_b32_e32 v34, s54
	s_andn2_b64 vcc, exec, s[6:7]
	s_waitcnt lgkmcnt(0)
	v_add_f32_e32 v35, v35, v36
	v_mov_b32_e32 v36, v35
	s_nop 1
	v_permlane32_swap_b32 v35, v36
	s_nop 1
	s_nop 0
	v_add_f32_e32 v35, v35, v36
	v_fmamk_f32 v35, v35, 0x3c800000, v0
	v_rsq_f32_e32 v36, v35
	v_mad_u64_u32 v[34:35], s[20:21], v57, 6, v[34:35]
	s_movk_i32 s20, 0x104
	s_nop 0
	v_mad_u64_u32 v[34:35], s[20:21], v34, s20, v[56:57]
	v_ashrrev_i32_e32 v35, 31, v34
	v_mul_f32_e32 v60, v191, v36
	v_lshlrev_b64 v[34:35], 14, v[34:35]
	v_lshlrev_b32_e32 v36, 4, v55
	v_lshl_add_u64 v[34:35], s[66:67], 0, v[34:35]
	v_and_b32_e32 v178, 0x2f0, v36
	v_lshl_add_u64 v[58:59], v[34:35], 0, v[178:179]
	v_pk_mul_f32 v[34:35], v[30:31], v[60:61] op_sel_hi:[1,0]
	v_pk_mul_f32 v[36:37], v[26:27], v[60:61] op_sel_hi:[1,0]
	v_pk_mul_f32 v[62:63], v[32:33], v[60:61] op_sel_hi:[1,0]
	v_pk_mul_f32 v[64:65], v[28:29], v[60:61] op_sel_hi:[1,0]
	v_pk_mul_f32 v[34:35], v[46:47], v[34:35]
	v_pk_mul_f32 v[36:37], v[50:51], v[36:37]
	v_pk_mul_f32 v[62:63], v[48:49], v[62:63]
	v_pk_mul_f32 v[64:65], v[52:53], v[64:65]
	v_cndmask_b32_e64 v61, 0, 1, s[6:7]
	v_cvt_pk_bf16_f32 v34, v34, v35
	v_cvt_pk_bf16_f32 v35, v62, v63
	v_cvt_pk_bf16_f32 v36, v36, v37
	v_cvt_pk_bf16_f32 v37, v64, v65
	v_cmp_ne_u32_e64 s[48:49], 1, v61
	s_mov_b64 s[20:21], -1
	s_cbranch_vccnz .LBB0_425
	v_mov_b32_e32 v169, v179
	v_lshl_add_u64 v[62:63], v[58:59], 0, v[168:169]
	s_mov_b64 s[20:21], 0
	global_store_dwordx4 v[62:63], v[34:37], off

; DEV unsigned cvtpk(float lo, float hi) { f32x2 v = {lo, hi}; bf16v2 r = __builtin_convertvector(v, bf16v2); return __builtin_bit_cast(unsigned, r); }
; DEV float fast_rsq(float x) { return __builtin_amdgcn_rsqf(x); }
; DEV float lx16(float v) { return __builtin_bit_cast(float, __builtin_amdgcn_ds_swizzle(__builtin_bit_cast(int, v), 0x401F)); }
; DEV float half_sum(float v) { float a, b; swap32(v, a, b); return a + b; }
;     DEV void operator()(const pg8::Acc& acc, const pg8::Unit& u, int wr, int wc, int fr, int fq) const {
;     ...
;                 } else {
;                     float ss = 0.f;
; #pragma unroll
;                     for (int bj = 0; bj < 2; ++bj)
; #pragma unroll
;                         for (int e = 0; e < 8; ++e) ss += x[bj][e] * x[bj][e];
;                     ss += lx16(ss); ss = half_sum(ss);
;                     const float rinv = fast_rsq(ss * (1.0f / 64.0f) + EPS);
;                     const float sc = rinv * (sect == 0 ? 0.125f * LOG2E : 1.0f);
; #pragma unroll
;                     for (int bj = 0; bj < 2; ++bj) { const f32x4 g0 = gq[bj][0], g1 = gq[bj][1]; float y[8];
; #pragma unroll
;                         for (int e = 0; e < 4; ++e) { y[e] = x[bj][e] * sc * g0[e]; y[4 + e] = x[bj][4 + e] * sc * g1[e]; }
;                         const u32x4 w = {cvtpk(y[0], y[1]), cvtpk(y[2], y[3]), cvtpk(y[4], y[5]), cvtpk(y[6], y[7])};
;                         if (sect == 0) *(u32x4*)((bf16_t*)(ws + WS_QB) + (size_t)tok * 384 + hd * 64 + 32 * bj + 8 * fq) = w;
;                         else *(u32x4*)(ws + WS_KVB + ((size_t)((b * 6 + hd) * 260 + (kidx >> 6))) * 16384 + (4 * bj + fq) * 1024 + (kidx & 63) * 16) = w; }
.LBB0_440:
	s_andn2_b64 vcc, exec, s[20:21]
	s_cbranch_vccnz .LBB0_453
	s_mov_b32 s20, 0x8000
	v_mov_b32_e32 v18, s55
	v_mov_b32_e32 v19, s58
	v_cmp_gt_i32_e32 vcc, s20, v22
	s_movk_i32 s20, 0x4000
	s_nop 0
	v_cndmask_b32_e32 v25, v18, v19, vcc
	v_and_b32_e32 v18, 0x3fff, v22
	v_or_b32_sdwa v19, v22, s20 dst_sel:DWORD dst_unused:UNUSED_PAD src0_sel:BYTE_0 src1_sel:DWORD
	v_cndmask_b32_e32 v23, v19, v18, vcc
	s_mov_b64 s[20:21], -1
	s_andn2_b64 vcc, exec, s[8:9]
	v_lshrrev_b32_e32 v24, 6, v23
	s_cbranch_vccnz .LBB0_451
	v_mul_f32_e32 v26, v15, v15
	v_fmac_f32_e32 v26, v14, v14
	v_fmac_f32_e32 v26, v16, v16
	v_fmac_f32_e32 v26, v17, v17
	v_fmac_f32_e32 v26, v10, v10
	v_fmac_f32_e32 v26, v11, v11
	v_fmac_f32_e32 v26, v12, v12
	v_fmac_f32_e32 v26, v13, v13
	v_fmac_f32_e32 v26, v6, v6
	v_fmac_f32_e32 v26, v7, v7
	v_fmac_f32_e32 v26, v8, v8
	v_fmac_f32_e32 v26, v9, v9
	v_pk_mul_f32 v[20:21], v[2:3], v[2:3]
	v_pk_mul_f32 v[18:19], v[4:5], v[4:5]
	v_add_f32_e32 v20, v20, v26
	v_add_f32_e32 v20, v21, v20
	v_add_f32_e32 v18, v18, v20
	v_add_f32_e32 v19, v19, v18
	ds_swizzle_b32 v20, v19 offset:swizzle(SWAP,16)
	v_mov_b32_e32 v18, s54
	s_andn2_b64 vcc, exec, s[6:7]
	s_waitcnt lgkmcnt(0)
	v_add_f32_e32 v19, v19, v20
	v_mov_b32_e32 v20, v19
	s_nop 1
	v_permlane32_swap_b32 v20, v19
	s_nop 1
	s_nop 0
	v_add_f32_e32 v19, v20, v19
	v_fmamk_f32 v19, v19, 0x3c800000, v0
	v_rsq_f32_e32 v20, v19
	v_mad_u64_u32 v[18:19], s[8:9], v25, 6, v[18:19]
	s_movk_i32 s8, 0x104
	s_nop 0
	v_mad_u64_u32 v[18:19], s[8:9], v18, s8, v[24:25]
	v_ashrrev_i32_e32 v19, 31, v18
	v_mul_f32_e32 v28, v191, v20
	v_lshlrev_b64 v[18:19], 14, v[18:19]
	v_lshlrev_b32_e32 v20, 4, v23
	v_lshl_add_u64 v[18:19], s[66:67], 0, v[18:19]
	v_and_b32_e32 v178, 0x3f0, v20
	v_lshl_add_u64 v[26:27], v[18:19], 0, v[178:179]
	v_pk_mul_f32 v[18:19], v[14:15], v[28:29] op_sel_hi:[1,0]
	v_pk_mul_f32 v[20:21], v[10:11], v[28:29] op_sel_hi:[1,0]
	v_pk_mul_f32 v[30:31], v[16:17], v[28:29] op_sel_hi:[1,0]
	v_pk_mul_f32 v[32:33], v[12:13], v[28:29] op_sel_hi:[1,0]
	v_pk_mul_f32 v[18:19], v[46:47], v[18:19]
	v_pk_mul_f32 v[20:21], v[50:51], v[20:21]
	v_pk_mul_f32 v[30:31], v[48:49], v[30:31]
	v_pk_mul_f32 v[32:33], v[52:53], v[32:33]
	v_cndmask_b32_e64 v29, 0, 1, s[6:7]
	v_cvt_pk_bf16_f32 v18, v18, v19
	v_cvt_pk_bf16_f32 v19, v30, v31
	v_cvt_pk_bf16_f32 v20, v20, v21
	v_cvt_pk_bf16_f32 v21, v32, v33
	v_cmp_ne_u32_e64 s[42:43], 1, v29
	s_mov_b64 s[6:7], -1
	s_cbranch_vccnz .LBB0_444
	v_mov_b32_e32 v169, v179
	v_lshl_add_u64 v[30:31], v[26:27], 0, v[168:169]
	s_mov_b64 s[6:7], 0
	global_store_dwordx4 v[30:31], v[18:21], off
